# up-GEMM epilogue: fp8 pack via op_sel hi-word converts instead of zero-init + and + shift-or (same values), on top of v109
# baseline (speedup 1.0000x reference)
.LBB0_1916:
	s_nop 15
	s_nop 15
	v_mov_b32_e32 v4, v166
	v_mov_b32_e32 v2, v167
	v_mov_b32_e32 v3, s24
	s_add_u32 s40, s2, 0xffffff00
	ds_read_b32 v3, v3 offset:288
	s_addc_u32 s41, s23, -1
	s_lshl_b32 s2, s31, 11
	s_add_i32 s2, s2, 0
	v_lshl_add_u32 v18, v2, 3, s83
	s_add_i32 s2, s2, 0x21000
	v_lshl_add_u32 v5, v18, 3, s2
	ds_read_b128 v[14:17], v5
	s_waitcnt lgkmcnt(1)
	v_readfirstlane_b32 s8, v3
	s_lshl_b32 s8, s8, 2
	s_add_i32 s8, s8, 0
	s_add_i32 s8, s8, 0x201c0
	v_mov_b32_e32 v2, s8
	ds_read2_b32 v[2:3], v2 offset1:32
	v_add_u32_e32 v19, s82, v4
	ds_read_b128 v[10:13], v5 offset:16
	ds_read_b128 v[6:9], v5 offset:32
	v_add_u32_e32 v22, 16, v19
	v_add_u32_e32 v24, 32, v19
	s_waitcnt lgkmcnt(2)
	v_readfirstlane_b32 s9, v2
	v_lshl_add_u32 v2, v19, 2, s2
	ds_read_b32 v20, v2 offset:1024
	v_readfirstlane_b32 s8, v3
	s_sub_i32 s8, s36, s8
	v_lshl_add_u32 v23, v22, 2, s2
	v_lshl_add_u32 v25, v24, 2, s2
	s_lshl_b32 s8, s8, 8
	ds_read_b128 v[2:5], v5 offset:48
	ds_read_b32 v23, v23 offset:1024
	ds_read_b32 v25, v25 offset:1024
	v_add_u32_e32 v21, s8, v19
	s_waitcnt lgkmcnt(3)
	v_mul_f32_e32 v20, 0x3b800000, v20
	v_cmp_gt_i32_e32 vcc, s9, v21
	s_waitcnt lgkmcnt(1)
	v_mul_f32_e32 v21, 0x3b800000, v23
	v_add_u32_e32 v26, 0xa0, v19
	v_cndmask_b32_e32 v180, 0, v20, vcc
	v_add_u32_e32 v20, s8, v22
	v_cmp_gt_i32_e32 vcc, s9, v20
	v_add_u32_e32 v20, s8, v24
	v_add_u32_e32 v22, 0x80, v19
	v_cndmask_b32_e32 v164, 0, v21, vcc
	s_waitcnt lgkmcnt(0)
	v_mul_f32_e32 v21, 0x3b800000, v25
	v_cmp_gt_i32_e32 vcc, s9, v20
	v_add_u32_e32 v20, 48, v19
	v_add_u32_e32 v24, 0x90, v19
	v_cndmask_b32_e32 v162, 0, v21, vcc
	v_lshl_add_u32 v21, v20, 2, s2
	v_lshl_add_u32 v23, v22, 2, s2
	v_lshl_add_u32 v25, v24, 2, s2
	v_lshl_add_u32 v27, v26, 2, s2
	v_add_u32_e32 v29, 0xb0, v19
	v_add_u32_e32 v20, s8, v20
	v_lshl_add_u32 v28, v29, 2, s2
	ds_read_b32 v21, v21 offset:1024
	ds_read_b32 v23, v23 offset:1024
	ds_read_b32 v25, v25 offset:1024
	ds_read_b32 v27, v27 offset:1024
	ds_read_b32 v31, v28 offset:1024
	s_waitcnt lgkmcnt(4)
	v_mul_f32_e32 v21, 0x3b800000, v21
	v_cmp_gt_i32_e32 vcc, s9, v20
	v_add_u32_e32 v20, s8, v22
	s_lshl_b32 s42, s14, 7
	v_cndmask_b32_e32 v32, 0, v21, vcc
	s_waitcnt lgkmcnt(3)
	v_mul_f32_e32 v21, 0x3b800000, v23
	v_cmp_gt_i32_e32 vcc, s9, v20
	v_add_u32_e32 v20, s8, v24
	v_mov_b32_e32 v24, v14
	v_cndmask_b32_e32 v30, 0, v21, vcc
	s_waitcnt lgkmcnt(2)
	v_mul_f32_e32 v21, 0x3b800000, v25
	v_mov_b32_e32 v25, v16
	v_pk_fma_f32 v[182:183], v[158:159], v[180:181], v[24:25] op_sel_hi:[1,0,1]
	v_mov_b32_e32 v16, v15
	v_min_f32_e32 v182, 0x40e00000, v182
	v_min_f32_e32 v183, 0x40e00000, v183
	v_pk_mul_f32 v[184:185], v[182:183], s[20:21] op_sel_hi:[1,0]
	v_cmp_gt_i32_e32 vcc, s9, v20
	v_exp_f32_e32 v184, v184
	v_exp_f32_e32 v185, v185
	v_add_u32_e32 v20, s8, v26
	v_cndmask_b32_e32 v28, 0, v21, vcc
	s_waitcnt lgkmcnt(1)
	v_mul_f32_e32 v21, 0x3b800000, v27
	v_pk_add_f32 v[14:15], v[184:185], 1.0 op_sel_hi:[1,0]
	v_pk_fma_f32 v[184:185], v[126:127], v[180:181], v[16:17] op_sel_hi:[1,0,1]
	v_rcp_f32_e32 v14, v14
	v_rcp_f32_e32 v15, v15
	v_med3_f32 v184, v184, s37, v176
	v_med3_f32 v185, v185, s37, v176
	v_cmp_gt_i32_e32 vcc, s9, v20
	v_pk_mul_f32 v[14:15], v[182:183], v[14:15]
	v_add_u32_e32 v20, s8, v29
	v_pk_fma_f32 v[182:183], v[184:185], v[14:15], v[14:15]
	v_mov_b32_e32 v14, v10
	v_mov_b32_e32 v15, v12
	v_pk_fma_f32 v[184:185], v[160:161], v[180:181], v[14:15] op_sel_hi:[1,0,1]
	v_mov_b32_e32 v12, v11
	v_min_f32_e32 v184, 0x40e00000, v184
	v_min_f32_e32 v185, 0x40e00000, v185
	v_pk_mul_f32 v[186:187], v[184:185], s[20:21] op_sel_hi:[1,0]
	v_cndmask_b32_e32 v26, 0, v21, vcc
	v_exp_f32_e32 v186, v186
	v_exp_f32_e32 v187, v187
	s_waitcnt lgkmcnt(0)
	v_mul_f32_e32 v21, 0x3b800000, v31
	v_cmp_gt_i32_e32 vcc, s9, v20
	v_pk_add_f32 v[10:11], v[186:187], 1.0 op_sel_hi:[1,0]
	v_cndmask_b32_e32 v22, 0, v21, vcc
	v_rcp_f32_e32 v10, v10
	v_rcp_f32_e32 v11, v11
	v_cvt_pk_fp8_f32 v21, v182, v183
	v_pk_fma_f32 v[182:183], v[128:129], v[180:181], v[12:13] op_sel_hi:[1,0,1]
	v_pk_mul_f32 v[10:11], v[184:185], v[10:11]
	v_med3_f32 v182, v182, s37, v176
	v_med3_f32 v183, v183, s37, v176
	v_pk_fma_f32 v[182:183], v[182:183], v[10:11], v[10:11]
	v_mov_b32_e32 v10, v6
	v_mov_b32_e32 v11, v8
	v_pk_fma_f32 v[184:185], v[154:155], v[180:181], v[10:11] op_sel_hi:[1,0,1]
	v_mov_b32_e32 v8, v7
	v_min_f32_e32 v184, 0x40e00000, v184
	v_min_f32_e32 v185, 0x40e00000, v185
	v_pk_mul_f32 v[186:187], v[184:185], s[20:21] op_sel_hi:[1,0]
	v_cvt_pk_fp8_f32 v21, v182, v183 op_sel:[0,0,1]
	v_exp_f32_e32 v186, v186
	v_exp_f32_e32 v187, v187
	v_pk_fma_f32 v[182:183], v[122:123], v[180:181], v[8:9] op_sel_hi:[1,0,1]
	v_med3_f32 v182, v182, s37, v176
	v_pk_add_f32 v[6:7], v[186:187], 1.0 op_sel_hi:[1,0]
	v_med3_f32 v183, v183, s37, v176
	v_rcp_f32_e32 v6, v6
	v_rcp_f32_e32 v7, v7
	v_lshl_add_u32 v20, s36, 8, v19
	s_ashr_i32 s43, s42, 31
	v_pk_mul_f32 v[6:7], v[184:185], v[6:7]
	v_ashrrev_i32_e32 v19, 31, v18
	v_pk_fma_f32 v[182:183], v[182:183], v[6:7], v[6:7]
	v_mov_b32_e32 v6, v2
	v_mov_b32_e32 v7, v4
	v_pk_fma_f32 v[184:185], v[156:157], v[180:181], v[6:7] op_sel_hi:[1,0,1]
	v_mov_b32_e32 v4, v3
	v_min_f32_e32 v184, 0x40e00000, v184
	v_min_f32_e32 v185, 0x40e00000, v185
	v_pk_mul_f32 v[186:187], v[184:185], s[20:21] op_sel_hi:[1,0]
	v_pk_fma_f32 v[180:181], v[124:125], v[180:181], v[4:5] op_sel_hi:[1,0,1]
	v_exp_f32_e32 v186, v186
	v_exp_f32_e32 v187, v187
	v_cvt_pk_fp8_f32 v27, v182, v183
	v_med3_f32 v180, v180, s37, v176
	v_med3_f32 v181, v181, s37, v176
	v_pk_add_f32 v[2:3], v[186:187], 1.0 op_sel_hi:[1,0]
	v_pk_fma_f32 v[182:183], v[150:151], v[164:165], v[24:25] op_sel_hi:[1,0,1]
	v_rcp_f32_e32 v2, v2
	v_rcp_f32_e32 v3, v3
	v_min_f32_e32 v182, 0x40e00000, v182
	v_min_f32_e32 v183, 0x40e00000, v183
	s_and_b64 vcc, exec, s[6:7]
	v_pk_mul_f32 v[2:3], v[184:185], v[2:3]
	v_pk_mul_f32 v[184:185], v[182:183], s[20:21] op_sel_hi:[1,0]
	v_pk_fma_f32 v[2:3], v[180:181], v[2:3], v[2:3]
	v_exp_f32_e32 v184, v184
	v_cvt_pk_fp8_f32 v27, v2, v3 op_sel:[0,0,1]
	v_mov_b32_e32 v2, v21
	v_ashrrev_i32_e32 v21, 31, v20
	v_lshlrev_b64 v[180:181], 10, v[20:21]
	v_exp_f32_e32 v185, v185
	v_lshl_add_u64 v[180:181], s[12:13], 0, v[180:181]
	v_mov_b32_e32 v3, v27
	v_lshl_add_u64 v[180:181], v[180:181], 0, s[42:43]
	v_lshl_add_u64 v[180:181], v[180:181], 0, v[18:19]
	global_store_dwordx2 v[180:181], v[2:3], off
	v_pk_add_f32 v[2:3], v[184:185], 1.0 op_sel_hi:[1,0]
	v_pk_fma_f32 v[180:181], v[118:119], v[164:165], v[16:17] op_sel_hi:[1,0,1]
	v_rcp_f32_e32 v2, v2
	v_rcp_f32_e32 v3, v3
	v_med3_f32 v180, v180, s37, v176
	v_med3_f32 v181, v181, s37, v176
	v_pk_mul_f32 v[2:3], v[182:183], v[2:3]
	v_pk_fma_f32 v[182:183], v[152:153], v[164:165], v[14:15] op_sel_hi:[1,0,1]
	v_pk_fma_f32 v[2:3], v[180:181], v[2:3], v[2:3]
	v_min_f32_e32 v182, 0x40e00000, v182
	v_min_f32_e32 v183, 0x40e00000, v183
	v_pk_mul_f32 v[184:185], v[182:183], s[20:21] op_sel_hi:[1,0]
	v_cvt_pk_fp8_f32 v21, v2, v3
	v_exp_f32_e32 v184, v184
	v_exp_f32_e32 v185, v185
	v_pk_fma_f32 v[180:181], v[120:121], v[164:165], v[12:13] op_sel_hi:[1,0,1]
	v_med3_f32 v180, v180, s37, v176
	v_pk_add_f32 v[2:3], v[184:185], 1.0 op_sel_hi:[1,0]
	v_med3_f32 v181, v181, s37, v176
	v_rcp_f32_e32 v2, v2
	v_rcp_f32_e32 v3, v3
	s_nop 0
	v_pk_mul_f32 v[2:3], v[182:183], v[2:3]
	v_pk_fma_f32 v[182:183], v[146:147], v[164:165], v[10:11] op_sel_hi:[1,0,1]
	v_pk_fma_f32 v[2:3], v[180:181], v[2:3], v[2:3]
	v_min_f32_e32 v182, 0x40e00000, v182
	v_min_f32_e32 v183, 0x40e00000, v183
	v_pk_mul_f32 v[184:185], v[182:183], s[20:21] op_sel_hi:[1,0]
	v_cvt_pk_fp8_f32 v21, v2, v3 op_sel:[0,0,1]
	v_exp_f32_e32 v184, v184
	v_exp_f32_e32 v185, v185
	v_pk_fma_f32 v[180:181], v[114:115], v[164:165], v[8:9] op_sel_hi:[1,0,1]
	v_pk_add_f32 v[2:3], v[184:185], 1.0 op_sel_hi:[1,0]
	s_nop 0
	v_rcp_f32_e32 v2, v2
	v_rcp_f32_e32 v3, v3
	v_med3_f32 v180, v180, s37, v176
	v_med3_f32 v181, v181, s37, v176
	v_pk_mul_f32 v[2:3], v[182:183], v[2:3]
	v_pk_fma_f32 v[182:183], v[148:149], v[164:165], v[6:7] op_sel_hi:[1,0,1]
	v_pk_fma_f32 v[2:3], v[180:181], v[2:3], v[2:3]
	v_min_f32_e32 v182, 0x40e00000, v182
	v_min_f32_e32 v183, 0x40e00000, v183
	v_pk_mul_f32 v[184:185], v[182:183], s[20:21] op_sel_hi:[1,0]
	v_cvt_pk_fp8_f32 v27, v2, v3
	v_exp_f32_e32 v184, v184
	v_exp_f32_e32 v185, v185
	v_pk_fma_f32 v[180:181], v[116:117], v[164:165], v[4:5] op_sel_hi:[1,0,1]
	v_pk_add_f32 v[2:3], v[184:185], 1.0 op_sel_hi:[1,0]
	s_nop 0
	v_rcp_f32_e32 v2, v2
	v_rcp_f32_e32 v3, v3
	v_med3_f32 v180, v180, s37, v176
	v_med3_f32 v181, v181, s37, v176
	v_pk_mul_f32 v[2:3], v[182:183], v[2:3]
	v_pk_fma_f32 v[182:183], v[142:143], v[162:163], v[24:25] op_sel_hi:[1,0,1]
	v_pk_fma_f32 v[2:3], v[180:181], v[2:3], v[2:3]
	v_add_u32_e32 v180, 16, v20
	v_min_f32_e32 v182, 0x40e00000, v182
	v_min_f32_e32 v183, 0x40e00000, v183
	v_cvt_pk_fp8_f32 v27, v2, v3 op_sel:[0,0,1]
	v_ashrrev_i32_e32 v181, 31, v180
	v_pk_mul_f32 v[184:185], v[182:183], s[20:21] op_sel_hi:[1,0]
	v_lshlrev_b64 v[180:181], 10, v[180:181]
	v_exp_f32_e32 v184, v184
	v_exp_f32_e32 v185, v185
	v_lshl_add_u64 v[180:181], s[12:13], 0, v[180:181]
	v_mov_b32_e32 v2, v21
	v_mov_b32_e32 v3, v27
	v_lshl_add_u64 v[180:181], v[180:181], 0, s[42:43]
	v_lshl_add_u64 v[180:181], v[180:181], 0, v[18:19]
	global_store_dwordx2 v[180:181], v[2:3], off
	v_pk_add_f32 v[2:3], v[184:185], 1.0 op_sel_hi:[1,0]
	v_pk_fma_f32 v[180:181], v[110:111], v[162:163], v[16:17] op_sel_hi:[1,0,1]
	v_rcp_f32_e32 v2, v2
	v_rcp_f32_e32 v3, v3
	v_med3_f32 v180, v180, s37, v176
	v_med3_f32 v181, v181, s37, v176
	v_pk_mul_f32 v[2:3], v[182:183], v[2:3]
	v_pk_fma_f32 v[182:183], v[144:145], v[162:163], v[14:15] op_sel_hi:[1,0,1]
	v_pk_fma_f32 v[2:3], v[180:181], v[2:3], v[2:3]
	v_min_f32_e32 v182, 0x40e00000, v182
	v_min_f32_e32 v183, 0x40e00000, v183
	v_pk_mul_f32 v[184:185], v[182:183], s[20:21] op_sel_hi:[1,0]
	v_cvt_pk_fp8_f32 v21, v2, v3
	v_exp_f32_e32 v184, v184
	v_exp_f32_e32 v185, v185
	v_pk_fma_f32 v[180:181], v[112:113], v[162:163], v[12:13] op_sel_hi:[1,0,1]
	v_med3_f32 v180, v180, s37, v176
	v_pk_add_f32 v[2:3], v[184:185], 1.0 op_sel_hi:[1,0]
	v_med3_f32 v181, v181, s37, v176
	v_rcp_f32_e32 v2, v2
	v_rcp_f32_e32 v3, v3
	s_nop 0
	v_pk_mul_f32 v[2:3], v[182:183], v[2:3]
	v_pk_fma_f32 v[182:183], v[138:139], v[162:163], v[10:11] op_sel_hi:[1,0,1]
	v_pk_fma_f32 v[2:3], v[180:181], v[2:3], v[2:3]
	v_min_f32_e32 v182, 0x40e00000, v182
	v_min_f32_e32 v183, 0x40e00000, v183
	v_pk_mul_f32 v[184:185], v[182:183], s[20:21] op_sel_hi:[1,0]
	v_cvt_pk_fp8_f32 v21, v2, v3 op_sel:[0,0,1]
	v_exp_f32_e32 v184, v184
	v_exp_f32_e32 v185, v185
	v_pk_fma_f32 v[180:181], v[106:107], v[162:163], v[8:9] op_sel_hi:[1,0,1]
	v_pk_add_f32 v[2:3], v[184:185], 1.0 op_sel_hi:[1,0]
	s_nop 0
	v_rcp_f32_e32 v2, v2
	v_rcp_f32_e32 v3, v3
	v_med3_f32 v180, v180, s37, v176
	v_med3_f32 v181, v181, s37, v176
	v_pk_mul_f32 v[2:3], v[182:183], v[2:3]
	v_pk_fma_f32 v[182:183], v[140:141], v[162:163], v[6:7] op_sel_hi:[1,0,1]
	v_pk_fma_f32 v[2:3], v[180:181], v[2:3], v[2:3]
	v_min_f32_e32 v182, 0x40e00000, v182
	v_min_f32_e32 v183, 0x40e00000, v183
	v_pk_mul_f32 v[184:185], v[182:183], s[20:21] op_sel_hi:[1,0]
	v_cvt_pk_fp8_f32 v27, v2, v3
	v_exp_f32_e32 v184, v184
	v_exp_f32_e32 v185, v185
	v_pk_fma_f32 v[180:181], v[108:109], v[162:163], v[4:5] op_sel_hi:[1,0,1]
	v_pk_add_f32 v[2:3], v[184:185], 1.0 op_sel_hi:[1,0]
	s_nop 0
	v_rcp_f32_e32 v2, v2
	v_rcp_f32_e32 v3, v3
	v_med3_f32 v180, v180, s37, v176
	v_med3_f32 v181, v181, s37, v176
	v_pk_mul_f32 v[2:3], v[182:183], v[2:3]
	v_pk_fma_f32 v[182:183], v[134:135], v[32:33], v[24:25] op_sel_hi:[1,0,1]
	v_pk_fma_f32 v[2:3], v[180:181], v[2:3], v[2:3]
	v_add_u32_e32 v180, 32, v20
	v_min_f32_e32 v182, 0x40e00000, v182
	v_min_f32_e32 v183, 0x40e00000, v183
	v_cvt_pk_fp8_f32 v27, v2, v3 op_sel:[0,0,1]
	v_ashrrev_i32_e32 v181, 31, v180
	v_pk_mul_f32 v[184:185], v[182:183], s[20:21] op_sel_hi:[1,0]
	v_lshlrev_b64 v[180:181], 10, v[180:181]
	v_exp_f32_e32 v184, v184
	v_exp_f32_e32 v185, v185
	v_lshl_add_u64 v[180:181], s[12:13], 0, v[180:181]
	v_mov_b32_e32 v2, v21
	v_mov_b32_e32 v3, v27
	v_lshl_add_u64 v[180:181], v[180:181], 0, s[42:43]
	v_lshl_add_u64 v[180:181], v[180:181], 0, v[18:19]
	global_store_dwordx2 v[180:181], v[2:3], off
	v_pk_add_f32 v[2:3], v[184:185], 1.0 op_sel_hi:[1,0]
	v_pk_fma_f32 v[180:181], v[102:103], v[32:33], v[16:17] op_sel_hi:[1,0,1]
	v_rcp_f32_e32 v2, v2
	v_rcp_f32_e32 v3, v3
	v_med3_f32 v180, v180, s37, v176
	v_med3_f32 v181, v181, s37, v176
	v_pk_mul_f32 v[2:3], v[182:183], v[2:3]
	v_pk_fma_f32 v[182:183], v[136:137], v[32:33], v[14:15] op_sel_hi:[1,0,1]
	v_pk_fma_f32 v[2:3], v[180:181], v[2:3], v[2:3]
	v_min_f32_e32 v182, 0x40e00000, v182
	v_min_f32_e32 v183, 0x40e00000, v183
	v_pk_mul_f32 v[184:185], v[182:183], s[20:21] op_sel_hi:[1,0]
	v_cvt_pk_fp8_f32 v21, v2, v3
	v_exp_f32_e32 v184, v184
	v_exp_f32_e32 v185, v185
	v_pk_fma_f32 v[180:181], v[104:105], v[32:33], v[12:13] op_sel_hi:[1,0,1]
	v_med3_f32 v180, v180, s37, v176
	v_pk_add_f32 v[2:3], v[184:185], 1.0 op_sel_hi:[1,0]
	v_med3_f32 v181, v181, s37, v176
	v_rcp_f32_e32 v2, v2
	v_rcp_f32_e32 v3, v3
	s_nop 0
	v_pk_mul_f32 v[2:3], v[182:183], v[2:3]
	v_pk_fma_f32 v[182:183], v[130:131], v[32:33], v[10:11] op_sel_hi:[1,0,1]
	v_pk_fma_f32 v[2:3], v[180:181], v[2:3], v[2:3]
	v_min_f32_e32 v182, 0x40e00000, v182
	v_min_f32_e32 v183, 0x40e00000, v183
	v_pk_mul_f32 v[184:185], v[182:183], s[20:21] op_sel_hi:[1,0]
	v_cvt_pk_fp8_f32 v21, v2, v3 op_sel:[0,0,1]
	v_exp_f32_e32 v184, v184
	v_exp_f32_e32 v185, v185
	v_pk_fma_f32 v[180:181], v[98:99], v[32:33], v[8:9] op_sel_hi:[1,0,1]
	v_pk_add_f32 v[2:3], v[184:185], 1.0 op_sel_hi:[1,0]
	s_nop 0
	v_rcp_f32_e32 v2, v2
	v_rcp_f32_e32 v3, v3
	v_med3_f32 v180, v180, s37, v176
	v_med3_f32 v181, v181, s37, v176
	v_pk_mul_f32 v[2:3], v[182:183], v[2:3]
	v_pk_fma_f32 v[182:183], v[132:133], v[32:33], v[6:7] op_sel_hi:[1,0,1]
	v_pk_fma_f32 v[2:3], v[180:181], v[2:3], v[2:3]
	v_min_f32_e32 v182, 0x40e00000, v182
	v_min_f32_e32 v183, 0x40e00000, v183
	v_pk_mul_f32 v[184:185], v[182:183], s[20:21] op_sel_hi:[1,0]
	v_cvt_pk_fp8_f32 v27, v2, v3
	v_exp_f32_e32 v184, v184
	v_exp_f32_e32 v185, v185
	v_pk_fma_f32 v[32:33], v[100:101], v[32:33], v[4:5] op_sel_hi:[1,0,1]
	v_pk_fma_f32 v[180:181], v[94:95], v[30:31], v[24:25] op_sel_hi:[1,0,1]
	v_med3_f32 v32, v32, s37, v176
	v_pk_add_f32 v[2:3], v[184:185], 1.0 op_sel_hi:[1,0]
	v_med3_f32 v33, v33, s37, v176
	v_rcp_f32_e32 v2, v2
	v_rcp_f32_e32 v3, v3
	v_min_f32_e32 v180, 0x40e00000, v180
	v_min_f32_e32 v181, 0x40e00000, v181
	v_pk_mul_f32 v[2:3], v[182:183], v[2:3]
	s_nop 0
	v_pk_fma_f32 v[2:3], v[32:33], v[2:3], v[2:3]
	v_add_u32_e32 v32, 48, v20
	v_cvt_pk_fp8_f32 v27, v2, v3 op_sel:[0,0,1]
	v_ashrrev_i32_e32 v33, 31, v32
	v_pk_mul_f32 v[182:183], v[180:181], s[20:21] op_sel_hi:[1,0]
	v_lshlrev_b64 v[32:33], 10, v[32:33]
	v_exp_f32_e32 v182, v182
	v_exp_f32_e32 v183, v183
	v_lshl_add_u64 v[32:33], s[12:13], 0, v[32:33]
	v_mov_b32_e32 v2, v21
	v_mov_b32_e32 v3, v27
	v_lshl_add_u64 v[32:33], v[32:33], 0, s[42:43]
	v_lshl_add_u64 v[32:33], v[32:33], 0, v[18:19]
	global_store_dwordx2 v[32:33], v[2:3], off
	v_pk_add_f32 v[32:33], v[182:183], 1.0 op_sel_hi:[1,0]
	v_pk_fma_f32 v[182:183], v[62:63], v[30:31], v[16:17] op_sel_hi:[1,0,1]
	v_rcp_f32_e32 v32, v32
	v_rcp_f32_e32 v33, v33
	v_med3_f32 v182, v182, s37, v176
	v_med3_f32 v183, v183, s37, v176
	v_pk_mul_f32 v[32:33], v[180:181], v[32:33]
	v_pk_fma_f32 v[180:181], v[96:97], v[30:31], v[14:15] op_sel_hi:[1,0,1]
	v_pk_fma_f32 v[32:33], v[182:183], v[32:33], v[32:33]
	v_min_f32_e32 v180, 0x40e00000, v180
	v_min_f32_e32 v181, 0x40e00000, v181
	v_pk_mul_f32 v[184:185], v[180:181], s[20:21] op_sel_hi:[1,0]
	v_cvt_pk_fp8_f32 v3, v32, v33
	v_exp_f32_e32 v184, v184
	v_exp_f32_e32 v185, v185
	v_pk_fma_f32 v[182:183], v[64:65], v[30:31], v[12:13] op_sel_hi:[1,0,1]
	v_med3_f32 v182, v182, s37, v176
	v_pk_add_f32 v[32:33], v[184:185], 1.0 op_sel_hi:[1,0]
	v_med3_f32 v183, v183, s37, v176
	v_rcp_f32_e32 v32, v32
	v_rcp_f32_e32 v33, v33
	v_add_u32_e32 v2, 0x80, v20
	v_pk_mul_f32 v[32:33], v[180:181], v[32:33]
	v_pk_fma_f32 v[180:181], v[90:91], v[30:31], v[10:11] op_sel_hi:[1,0,1]
	v_pk_fma_f32 v[32:33], v[182:183], v[32:33], v[32:33]
	v_min_f32_e32 v180, 0x40e00000, v180
	v_min_f32_e32 v181, 0x40e00000, v181
	v_pk_mul_f32 v[184:185], v[180:181], s[20:21] op_sel_hi:[1,0]
	v_cvt_pk_fp8_f32 v3, v32, v33 op_sel:[0,0,1]
	v_exp_f32_e32 v184, v184
	v_exp_f32_e32 v185, v185
	v_pk_fma_f32 v[182:183], v[58:59], v[30:31], v[8:9] op_sel_hi:[1,0,1]
	v_med3_f32 v182, v182, s37, v176
	v_pk_add_f32 v[32:33], v[184:185], 1.0 op_sel_hi:[1,0]
	v_med3_f32 v183, v183, s37, v176
	v_rcp_f32_e32 v32, v32
	v_rcp_f32_e32 v33, v33
	s_nop 0
	v_pk_mul_f32 v[32:33], v[180:181], v[32:33]
	v_pk_fma_f32 v[180:181], v[92:93], v[30:31], v[6:7] op_sel_hi:[1,0,1]
	v_pk_fma_f32 v[32:33], v[182:183], v[32:33], v[32:33]
	v_min_f32_e32 v180, 0x40e00000, v180
	v_min_f32_e32 v181, 0x40e00000, v181
	v_pk_mul_f32 v[184:185], v[180:181], s[20:21] op_sel_hi:[1,0]
	v_cvt_pk_fp8_f32 v23, v32, v33
	v_exp_f32_e32 v184, v184
	v_exp_f32_e32 v185, v185
	v_pk_fma_f32 v[30:31], v[60:61], v[30:31], v[4:5] op_sel_hi:[1,0,1]
	v_med3_f32 v30, v30, s37, v176
	v_pk_add_f32 v[32:33], v[184:185], 1.0 op_sel_hi:[1,0]
	v_med3_f32 v31, v31, s37, v176
	v_rcp_f32_e32 v32, v32
	v_rcp_f32_e32 v33, v33
	s_nop 0
	v_pk_mul_f32 v[32:33], v[180:181], v[32:33]
	s_nop 0
	v_pk_fma_f32 v[30:31], v[30:31], v[32:33], v[32:33]
	v_pk_fma_f32 v[32:33], v[86:87], v[28:29], v[24:25] op_sel_hi:[1,0,1]
	v_cvt_pk_fp8_f32 v23, v30, v31 op_sel:[0,0,1]
	v_min_f32_e32 v32, 0x40e00000, v32
	v_min_f32_e32 v33, 0x40e00000, v33
	v_mov_b32_e32 v30, v3
	v_ashrrev_i32_e32 v3, 31, v2
	v_pk_mul_f32 v[180:181], v[32:33], s[20:21] op_sel_hi:[1,0]
	v_lshlrev_b64 v[2:3], 10, v[2:3]
	v_exp_f32_e32 v180, v180
	v_exp_f32_e32 v181, v181
	v_lshl_add_u64 v[2:3], s[12:13], 0, v[2:3]
	v_lshl_add_u64 v[2:3], v[2:3], 0, s[42:43]
	v_mov_b32_e32 v31, v23
	v_lshl_add_u64 v[2:3], v[2:3], 0, v[18:19]
	global_store_dwordx2 v[2:3], v[30:31], off
	v_pk_add_f32 v[2:3], v[180:181], 1.0 op_sel_hi:[1,0]
	v_pk_fma_f32 v[30:31], v[54:55], v[28:29], v[16:17] op_sel_hi:[1,0,1]
	v_rcp_f32_e32 v2, v2
	v_rcp_f32_e32 v3, v3
	v_med3_f32 v30, v30, s37, v176
	v_med3_f32 v31, v31, s37, v176
	v_pk_mul_f32 v[2:3], v[32:33], v[2:3]
	v_pk_fma_f32 v[32:33], v[88:89], v[28:29], v[14:15] op_sel_hi:[1,0,1]
	v_pk_fma_f32 v[2:3], v[30:31], v[2:3], v[2:3]
	v_min_f32_e32 v32, 0x40e00000, v32
	v_min_f32_e32 v33, 0x40e00000, v33
	v_pk_mul_f32 v[180:181], v[32:33], s[20:21] op_sel_hi:[1,0]
	v_cvt_pk_fp8_f32 v21, v2, v3
	v_exp_f32_e32 v180, v180
	v_exp_f32_e32 v181, v181
	v_pk_fma_f32 v[30:31], v[56:57], v[28:29], v[12:13] op_sel_hi:[1,0,1]
	v_med3_f32 v30, v30, s37, v176
	v_pk_add_f32 v[2:3], v[180:181], 1.0 op_sel_hi:[1,0]
	v_med3_f32 v31, v31, s37, v176
	v_rcp_f32_e32 v2, v2
	v_rcp_f32_e32 v3, v3
	s_nop 0
	v_pk_mul_f32 v[2:3], v[32:33], v[2:3]
	v_pk_fma_f32 v[32:33], v[82:83], v[28:29], v[10:11] op_sel_hi:[1,0,1]
	v_pk_fma_f32 v[2:3], v[30:31], v[2:3], v[2:3]
	v_min_f32_e32 v32, 0x40e00000, v32
	v_min_f32_e32 v33, 0x40e00000, v33
	v_pk_mul_f32 v[180:181], v[32:33], s[20:21] op_sel_hi:[1,0]
	v_cvt_pk_fp8_f32 v21, v2, v3 op_sel:[0,0,1]
	v_exp_f32_e32 v180, v180
	v_exp_f32_e32 v181, v181
	v_pk_fma_f32 v[30:31], v[50:51], v[28:29], v[8:9] op_sel_hi:[1,0,1]
	v_pk_add_f32 v[2:3], v[180:181], 1.0 op_sel_hi:[1,0]
	s_nop 0
	v_rcp_f32_e32 v2, v2
	v_rcp_f32_e32 v3, v3
	v_med3_f32 v30, v30, s37, v176
	v_med3_f32 v31, v31, s37, v176
	v_pk_mul_f32 v[2:3], v[32:33], v[2:3]
	v_pk_fma_f32 v[32:33], v[84:85], v[28:29], v[6:7] op_sel_hi:[1,0,1]
	v_pk_fma_f32 v[2:3], v[30:31], v[2:3], v[2:3]
	v_min_f32_e32 v32, 0x40e00000, v32
	v_min_f32_e32 v33, 0x40e00000, v33
	v_pk_mul_f32 v[180:181], v[32:33], s[20:21] op_sel_hi:[1,0]
	v_cvt_pk_fp8_f32 v27, v2, v3
	v_exp_f32_e32 v180, v180
	v_exp_f32_e32 v181, v181
	v_pk_fma_f32 v[28:29], v[52:53], v[28:29], v[4:5] op_sel_hi:[1,0,1]
	v_pk_fma_f32 v[30:31], v[78:79], v[26:27], v[24:25] op_sel_hi:[1,0,1]
	v_med3_f32 v28, v28, s37, v176
	v_pk_add_f32 v[2:3], v[180:181], 1.0 op_sel_hi:[1,0]
	v_med3_f32 v29, v29, s37, v176
	v_rcp_f32_e32 v2, v2
	v_rcp_f32_e32 v3, v3
	v_min_f32_e32 v30, 0x40e00000, v30
	v_min_f32_e32 v31, 0x40e00000, v31
	v_pk_mul_f32 v[2:3], v[32:33], v[2:3]
	s_nop 0
	v_pk_fma_f32 v[2:3], v[28:29], v[2:3], v[2:3]
	v_cvt_pk_fp8_f32 v27, v2, v3 op_sel:[0,0,1]
	s_nop 0
	v_mov_b32_e32 v3, v27
	v_pk_mul_f32 v[32:33], v[30:31], s[20:21] op_sel_hi:[1,0]
	v_mov_b32_e32 v2, v21
	v_add_u32_e32 v28, 0x90, v20
	v_ashrrev_i32_e32 v29, 31, v28
	v_lshlrev_b64 v[28:29], 10, v[28:29]
	v_exp_f32_e32 v32, v32
	v_exp_f32_e32 v33, v33
	v_lshl_add_u64 v[28:29], s[12:13], 0, v[28:29]
	v_lshl_add_u64 v[28:29], v[28:29], 0, s[42:43]
	v_lshl_add_u64 v[28:29], v[28:29], 0, v[18:19]
	global_store_dwordx2 v[28:29], v[2:3], off
	v_pk_add_f32 v[2:3], v[32:33], 1.0 op_sel_hi:[1,0]
	v_pk_fma_f32 v[28:29], v[46:47], v[26:27], v[16:17] op_sel_hi:[1,0,1]
	v_rcp_f32_e32 v2, v2
	v_rcp_f32_e32 v3, v3
	v_med3_f32 v28, v28, s37, v176
	v_med3_f32 v29, v29, s37, v176
	v_pk_mul_f32 v[2:3], v[30:31], v[2:3]
	v_pk_fma_f32 v[30:31], v[80:81], v[26:27], v[14:15] op_sel_hi:[1,0,1]
	v_pk_fma_f32 v[2:3], v[28:29], v[2:3], v[2:3]
	v_min_f32_e32 v30, 0x40e00000, v30
	v_min_f32_e32 v31, 0x40e00000, v31
	v_pk_mul_f32 v[32:33], v[30:31], s[20:21] op_sel_hi:[1,0]
	v_cvt_pk_fp8_f32 v21, v2, v3
	v_exp_f32_e32 v32, v32
	v_exp_f32_e32 v33, v33
	v_pk_fma_f32 v[28:29], v[48:49], v[26:27], v[12:13] op_sel_hi:[1,0,1]
	v_med3_f32 v28, v28, s37, v176
	v_pk_add_f32 v[2:3], v[32:33], 1.0 op_sel_hi:[1,0]
	v_med3_f32 v29, v29, s37, v176
	v_rcp_f32_e32 v2, v2
	v_rcp_f32_e32 v3, v3
	s_nop 0
	v_pk_mul_f32 v[2:3], v[30:31], v[2:3]
	v_pk_fma_f32 v[30:31], v[74:75], v[26:27], v[10:11] op_sel_hi:[1,0,1]
	v_pk_fma_f32 v[2:3], v[28:29], v[2:3], v[2:3]
	v_min_f32_e32 v30, 0x40e00000, v30
	v_min_f32_e32 v31, 0x40e00000, v31
	v_pk_mul_f32 v[32:33], v[30:31], s[20:21] op_sel_hi:[1,0]
	v_cvt_pk_fp8_f32 v21, v2, v3 op_sel:[0,0,1]
	v_exp_f32_e32 v32, v32
	v_exp_f32_e32 v33, v33
	v_pk_fma_f32 v[28:29], v[42:43], v[26:27], v[8:9] op_sel_hi:[1,0,1]
	v_pk_fma_f32 v[24:25], v[70:71], v[22:23], v[24:25] op_sel_hi:[1,0,1]
	v_med3_f32 v28, v28, s37, v176
	v_pk_add_f32 v[2:3], v[32:33], 1.0 op_sel_hi:[1,0]
	v_med3_f32 v29, v29, s37, v176
	v_rcp_f32_e32 v2, v2
	v_rcp_f32_e32 v3, v3
	v_min_f32_e32 v24, 0x40e00000, v24
	v_min_f32_e32 v25, 0x40e00000, v25
	v_pk_fma_f32 v[14:15], v[72:73], v[22:23], v[14:15] op_sel_hi:[1,0,1]
	v_pk_mul_f32 v[2:3], v[30:31], v[2:3]
	v_pk_fma_f32 v[30:31], v[76:77], v[26:27], v[6:7] op_sel_hi:[1,0,1]
	v_pk_fma_f32 v[2:3], v[28:29], v[2:3], v[2:3]
	v_min_f32_e32 v30, 0x40e00000, v30
	v_min_f32_e32 v31, 0x40e00000, v31
	v_pk_mul_f32 v[32:33], v[30:31], s[20:21] op_sel_hi:[1,0]
	v_exp_f32_e32 v32, v32
	v_exp_f32_e32 v33, v33
	v_cvt_pk_fp8_f32 v28, v2, v3
	v_pk_fma_f32 v[26:27], v[44:45], v[26:27], v[4:5] op_sel_hi:[1,0,1]
	v_min_f32_e32 v14, 0x40e00000, v14
	v_pk_add_f32 v[2:3], v[32:33], 1.0 op_sel_hi:[1,0]
	v_med3_f32 v26, v26, s37, v176
	v_rcp_f32_e32 v2, v2
	v_rcp_f32_e32 v3, v3
	v_med3_f32 v27, v27, s37, v176
	v_min_f32_e32 v15, 0x40e00000, v15
	v_pk_fma_f32 v[16:17], v[38:39], v[22:23], v[16:17] op_sel_hi:[1,0,1]
	v_pk_mul_f32 v[2:3], v[30:31], v[2:3]
	v_med3_f32 v16, v16, s37, v176
	v_pk_fma_f32 v[2:3], v[26:27], v[2:3], v[2:3]
	v_cvt_pk_fp8_f32 v28, v2, v3 op_sel:[0,0,1]
	s_nop 0
	v_mov_b32_e32 v3, v28
	v_pk_mul_f32 v[28:29], v[24:25], s[20:21] op_sel_hi:[1,0]
	v_mov_b32_e32 v2, v21
	v_add_u32_e32 v26, 0xa0, v20
	v_ashrrev_i32_e32 v27, 31, v26
	v_lshlrev_b64 v[26:27], 10, v[26:27]
	v_exp_f32_e32 v28, v28
	v_exp_f32_e32 v29, v29
	v_lshl_add_u64 v[26:27], s[12:13], 0, v[26:27]
	v_lshl_add_u64 v[26:27], v[26:27], 0, s[42:43]
	v_lshl_add_u64 v[26:27], v[26:27], 0, v[18:19]
	global_store_dwordx2 v[26:27], v[2:3], off
	v_pk_add_f32 v[2:3], v[28:29], 1.0 op_sel_hi:[1,0]
	v_med3_f32 v17, v17, s37, v176
	v_rcp_f32_e32 v2, v2
	v_rcp_f32_e32 v3, v3
	v_pk_fma_f32 v[10:11], v[66:67], v[22:23], v[10:11] op_sel_hi:[1,0,1]
	v_pk_fma_f32 v[12:13], v[40:41], v[22:23], v[12:13] op_sel_hi:[1,0,1]
	v_min_f32_e32 v10, 0x40e00000, v10
	v_pk_mul_f32 v[2:3], v[24:25], v[2:3]
	v_pk_mul_f32 v[24:25], v[14:15], s[20:21] op_sel_hi:[1,0]
	v_pk_fma_f32 v[2:3], v[16:17], v[2:3], v[2:3]
	v_exp_f32_e32 v24, v24
	v_exp_f32_e32 v25, v25
	v_cvt_pk_fp8_f32 v16, v2, v3
	v_min_f32_e32 v11, 0x40e00000, v11
	v_pk_add_f32 v[2:3], v[24:25], 1.0 op_sel_hi:[1,0]
	v_med3_f32 v12, v12, s37, v176
	v_rcp_f32_e32 v2, v2
	v_rcp_f32_e32 v3, v3
	v_med3_f32 v13, v13, s37, v176
	v_pk_fma_f32 v[6:7], v[68:69], v[22:23], v[6:7] op_sel_hi:[1,0,1]
	v_pk_fma_f32 v[8:9], v[34:35], v[22:23], v[8:9] op_sel_hi:[1,0,1]
	v_pk_mul_f32 v[2:3], v[14:15], v[2:3]
	v_pk_mul_f32 v[14:15], v[10:11], s[20:21] op_sel_hi:[1,0]
	v_pk_fma_f32 v[2:3], v[12:13], v[2:3], v[2:3]
	v_exp_f32_e32 v14, v14
	v_exp_f32_e32 v15, v15
	v_cvt_pk_fp8_f32 v16, v2, v3 op_sel:[0,0,1]
	v_min_f32_e32 v6, 0x40e00000, v6
	v_pk_add_f32 v[2:3], v[14:15], 1.0 op_sel_hi:[1,0]
	v_min_f32_e32 v7, 0x40e00000, v7
	v_rcp_f32_e32 v2, v2
	v_rcp_f32_e32 v3, v3
	v_med3_f32 v8, v8, s37, v176
	v_med3_f32 v9, v9, s37, v176
	v_pk_fma_f32 v[4:5], v[36:37], v[22:23], v[4:5] op_sel_hi:[1,0,1]
	v_pk_mul_f32 v[2:3], v[10:11], v[2:3]
	v_pk_mul_f32 v[10:11], v[6:7], s[20:21] op_sel_hi:[1,0]
	v_pk_fma_f32 v[2:3], v[8:9], v[2:3], v[2:3]
	v_exp_f32_e32 v10, v10
	v_exp_f32_e32 v11, v11
	v_cvt_pk_fp8_f32 v8, v2, v3
	v_med3_f32 v4, v4, s37, v176
	v_pk_add_f32 v[2:3], v[10:11], 1.0 op_sel_hi:[1,0]
	v_med3_f32 v5, v5, s37, v176
	v_rcp_f32_e32 v2, v2
	v_rcp_f32_e32 v3, v3
	s_nop 0
	v_pk_mul_f32 v[2:3], v[6:7], v[2:3]
	s_nop 0
	v_pk_fma_f32 v[2:3], v[4:5], v[2:3], v[2:3]
	v_cvt_pk_fp8_f32 v8, v2, v3 op_sel:[0,0,1]
	s_nop 0
	v_mov_b32_e32 v3, v8
	v_mov_b32_e32 v2, v16
	v_add_u32_e32 v4, 0xb0, v20
	v_ashrrev_i32_e32 v5, 31, v4
	v_lshlrev_b64 v[4:5], 10, v[4:5]
	v_lshl_add_u64 v[4:5], s[12:13], 0, v[4:5]
	v_lshl_add_u64 v[4:5], v[4:5], 0, s[42:43]
	v_lshl_add_u64 v[4:5], v[4:5], 0, v[18:19]
	global_store_dwordx2 v[4:5], v[2:3], off
	s_cbranch_vccnz .LBB0_1920
	s_andn2_b64 vcc, exec, s[0:1]
	s_cbranch_vccnz .LBB0_1919
	s_barrier

.LBB0_1959:
	s_nop 15
	s_nop 15
	v_mov_b32_e32 v4, v169
	v_mov_b32_e32 v2, v170
	v_mov_b32_e32 v3, s25
	ds_read_b32 v3, v3 offset:288
	s_lshl_b32 s8, s85, 11
	s_add_i32 s8, s8, 0
	v_lshl_add_u32 v18, v2, 3, s65
	s_add_i32 s8, s8, 0x21000
	v_lshl_add_u32 v5, v18, 3, s8
	ds_read_b128 v[14:17], v5
	s_waitcnt lgkmcnt(1)
	v_readfirstlane_b32 s9, v3
	s_lshl_b32 s9, s9, 2
	s_add_i32 s9, s9, 0
	s_add_i32 s9, s9, 0x201c0
	v_mov_b32_e32 v2, s9
	ds_read2_b32 v[2:3], v2 offset1:32
	v_add_u32_e32 v19, s64, v4
	ds_read_b128 v[10:13], v5 offset:16
	ds_read_b128 v[6:9], v5 offset:32
	v_add_u32_e32 v22, 16, v19
	v_add_u32_e32 v24, 32, v19
	s_waitcnt lgkmcnt(2)
	v_readfirstlane_b32 s23, v2
	v_lshl_add_u32 v2, v19, 2, s8
	ds_read_b32 v20, v2 offset:1024
	v_readfirstlane_b32 s9, v3
	s_sub_i32 s9, s2, s9
	v_lshl_add_u32 v23, v22, 2, s8
	v_lshl_add_u32 v25, v24, 2, s8
	s_lshl_b32 s9, s9, 8
	ds_read_b128 v[2:5], v5 offset:48
	ds_read_b32 v23, v23 offset:1024
	ds_read_b32 v25, v25 offset:1024
	v_add_u32_e32 v21, s9, v19
	s_waitcnt lgkmcnt(3)
	v_mul_f32_e32 v20, 0x3b800000, v20
	v_cmp_gt_i32_e32 vcc, s23, v21
	s_waitcnt lgkmcnt(1)
	v_mul_f32_e32 v21, 0x3b800000, v23
	v_add_u32_e32 v26, 0xa0, v19
	v_cndmask_b32_e32 v180, 0, v20, vcc
	v_add_u32_e32 v20, s9, v22
	v_cmp_gt_i32_e32 vcc, s23, v20
	v_add_u32_e32 v20, s9, v24
	v_add_u32_e32 v22, 0x80, v19
	v_cndmask_b32_e32 v166, 0, v21, vcc
	s_waitcnt lgkmcnt(0)
	v_mul_f32_e32 v21, 0x3b800000, v25
	v_cmp_gt_i32_e32 vcc, s23, v20
	v_add_u32_e32 v20, 48, v19
	v_add_u32_e32 v24, 0x90, v19
	v_cndmask_b32_e32 v164, 0, v21, vcc
	v_lshl_add_u32 v21, v20, 2, s8
	v_lshl_add_u32 v23, v22, 2, s8
	v_lshl_add_u32 v25, v24, 2, s8
	v_lshl_add_u32 v27, v26, 2, s8
	v_add_u32_e32 v29, 0xb0, v19
	v_add_u32_e32 v20, s9, v20
	v_lshl_add_u32 v28, v29, 2, s8
	ds_read_b32 v21, v21 offset:1024
	ds_read_b32 v23, v23 offset:1024
	ds_read_b32 v25, v25 offset:1024
	ds_read_b32 v27, v27 offset:1024
	ds_read_b32 v31, v28 offset:1024
	s_waitcnt lgkmcnt(4)
	v_mul_f32_e32 v21, 0x3b800000, v21
	v_cmp_gt_i32_e32 vcc, s23, v20
	v_add_u32_e32 v20, s9, v22
	s_lshl_b32 s26, s26, 7
	v_cndmask_b32_e32 v32, 0, v21, vcc
	s_waitcnt lgkmcnt(3)
	v_mul_f32_e32 v21, 0x3b800000, v23
	v_cmp_gt_i32_e32 vcc, s23, v20
	v_add_u32_e32 v20, s9, v24
	v_mov_b32_e32 v24, v14
	v_cndmask_b32_e32 v30, 0, v21, vcc
	s_waitcnt lgkmcnt(2)
	v_mul_f32_e32 v21, 0x3b800000, v25
	v_mov_b32_e32 v25, v16
	v_pk_fma_f32 v[158:159], v[158:159], v[180:181], v[24:25] op_sel_hi:[1,0,1]
	v_mov_b32_e32 v16, v15
	v_min_f32_e32 v158, 0x40e00000, v158
	v_min_f32_e32 v159, 0x40e00000, v159
	v_pk_mul_f32 v[182:183], v[158:159], s[20:21] op_sel_hi:[1,0]
	v_pk_fma_f32 v[154:155], v[154:155], v[180:181], v[16:17] op_sel_hi:[1,0,1]
	v_exp_f32_e32 v182, v182
	v_exp_f32_e32 v183, v183
	v_med3_f32 v154, v154, s82, v176
	v_med3_f32 v155, v155, s82, v176
	v_cmp_gt_i32_e32 vcc, s23, v20
	v_pk_add_f32 v[14:15], v[182:183], 1.0 op_sel_hi:[1,0]
	v_add_u32_e32 v20, s9, v26
	v_rcp_f32_e32 v14, v14
	v_rcp_f32_e32 v15, v15
	v_cndmask_b32_e32 v28, 0, v21, vcc
	s_waitcnt lgkmcnt(1)
	v_mul_f32_e32 v21, 0x3b800000, v27
	v_cmp_gt_i32_e32 vcc, s23, v20
	v_pk_mul_f32 v[14:15], v[158:159], v[14:15]
	v_add_u32_e32 v20, s9, v29
	v_pk_fma_f32 v[154:155], v[154:155], v[14:15], v[14:15]
	v_mov_b32_e32 v14, v10
	v_mov_b32_e32 v15, v12
	v_pk_fma_f32 v[158:159], v[160:161], v[180:181], v[14:15] op_sel_hi:[1,0,1]
	v_mov_b32_e32 v12, v11
	v_min_f32_e32 v158, 0x40e00000, v158
	v_min_f32_e32 v159, 0x40e00000, v159
	v_pk_mul_f32 v[160:161], v[158:159], s[20:21] op_sel_hi:[1,0]
	v_cndmask_b32_e32 v26, 0, v21, vcc
	v_exp_f32_e32 v160, v160
	v_exp_f32_e32 v161, v161
	s_waitcnt lgkmcnt(0)
	v_mul_f32_e32 v21, 0x3b800000, v31
	v_cmp_gt_i32_e32 vcc, s23, v20
	v_pk_add_f32 v[10:11], v[160:161], 1.0 op_sel_hi:[1,0]
	v_cndmask_b32_e32 v22, 0, v21, vcc
	v_rcp_f32_e32 v10, v10
	v_rcp_f32_e32 v11, v11
	v_cvt_pk_fp8_f32 v21, v154, v155
	v_pk_fma_f32 v[154:155], v[156:157], v[180:181], v[12:13] op_sel_hi:[1,0,1]
	v_pk_mul_f32 v[10:11], v[158:159], v[10:11]
	v_med3_f32 v154, v154, s82, v176
	v_med3_f32 v155, v155, s82, v176
	v_pk_fma_f32 v[154:155], v[154:155], v[10:11], v[10:11]
	v_mov_b32_e32 v10, v6
	v_mov_b32_e32 v11, v8
	v_pk_fma_f32 v[150:151], v[150:151], v[180:181], v[10:11] op_sel_hi:[1,0,1]
	v_mov_b32_e32 v8, v7
	v_min_f32_e32 v150, 0x40e00000, v150
	v_min_f32_e32 v151, 0x40e00000, v151
	v_pk_mul_f32 v[156:157], v[150:151], s[20:21] op_sel_hi:[1,0]
	v_pk_fma_f32 v[146:147], v[146:147], v[180:181], v[8:9] op_sel_hi:[1,0,1]
	v_exp_f32_e32 v156, v156
	v_exp_f32_e32 v157, v157
	v_med3_f32 v146, v146, s82, v176
	v_med3_f32 v147, v147, s82, v176
	v_pk_fma_f32 v[142:143], v[142:143], v[166:167], v[24:25] op_sel_hi:[1,0,1]
	v_pk_add_f32 v[6:7], v[156:157], 1.0 op_sel_hi:[1,0]
	v_lshl_add_u32 v20, s2, 8, v19
	v_rcp_f32_e32 v6, v6
	v_rcp_f32_e32 v7, v7
	v_min_f32_e32 v142, 0x40e00000, v142
	v_pk_mul_f32 v[6:7], v[150:151], v[6:7]
	v_min_f32_e32 v143, 0x40e00000, v143
	v_pk_fma_f32 v[146:147], v[146:147], v[6:7], v[6:7]
	v_mov_b32_e32 v6, v2
	v_mov_b32_e32 v7, v4
	v_pk_fma_f32 v[150:151], v[152:153], v[180:181], v[6:7] op_sel_hi:[1,0,1]
	v_mov_b32_e32 v4, v3
	v_min_f32_e32 v150, 0x40e00000, v150
	v_min_f32_e32 v151, 0x40e00000, v151
	v_pk_mul_f32 v[152:153], v[150:151], s[20:21] op_sel_hi:[1,0]
	v_cvt_pk_fp8_f32 v27, v146, v147
	v_exp_f32_e32 v152, v152
	v_exp_f32_e32 v153, v153
	v_pk_fma_f32 v[146:147], v[148:149], v[180:181], v[4:5] op_sel_hi:[1,0,1]
	v_cvt_pk_fp8_f32 v21, v154, v155 op_sel:[0,0,1]
	v_med3_f32 v146, v146, s82, v176
	v_pk_add_f32 v[2:3], v[152:153], 1.0 op_sel_hi:[1,0]
	v_med3_f32 v147, v147, s82, v176
	v_rcp_f32_e32 v2, v2
	v_rcp_f32_e32 v3, v3
	v_pk_mul_f32 v[148:149], v[142:143], s[20:21] op_sel_hi:[1,0]
	s_ashr_i32 s27, s26, 31
	v_exp_f32_e32 v148, v148
	v_pk_mul_f32 v[2:3], v[150:151], v[2:3]
	v_exp_f32_e32 v149, v149
	v_pk_fma_f32 v[2:3], v[146:147], v[2:3], v[2:3]
	v_ashrrev_i32_e32 v19, 31, v18
	v_cvt_pk_fp8_f32 v27, v2, v3 op_sel:[0,0,1]
	v_mov_b32_e32 v2, v21
	v_ashrrev_i32_e32 v21, 31, v20
	v_lshlrev_b64 v[146:147], 10, v[20:21]
	v_lshl_add_u64 v[146:147], s[12:13], 0, v[146:147]
	v_mov_b32_e32 v3, v27
	v_lshl_add_u64 v[146:147], v[146:147], 0, s[26:27]
	v_lshl_add_u64 v[146:147], v[146:147], 0, v[18:19]
	global_store_dwordx2 v[146:147], v[2:3], off
	v_pk_add_f32 v[2:3], v[148:149], 1.0 op_sel_hi:[1,0]
	v_pk_fma_f32 v[138:139], v[138:139], v[166:167], v[16:17] op_sel_hi:[1,0,1]
	v_rcp_f32_e32 v2, v2
	v_rcp_f32_e32 v3, v3
	v_med3_f32 v138, v138, s82, v176
	v_med3_f32 v139, v139, s82, v176
	v_pk_mul_f32 v[2:3], v[142:143], v[2:3]
	v_pk_fma_f32 v[142:143], v[144:145], v[166:167], v[14:15] op_sel_hi:[1,0,1]
	v_pk_fma_f32 v[2:3], v[138:139], v[2:3], v[2:3]
	v_min_f32_e32 v142, 0x40e00000, v142
	v_min_f32_e32 v143, 0x40e00000, v143
	v_pk_mul_f32 v[144:145], v[142:143], s[20:21] op_sel_hi:[1,0]
	v_cvt_pk_fp8_f32 v21, v2, v3
	v_exp_f32_e32 v144, v144
	v_exp_f32_e32 v145, v145
	v_pk_fma_f32 v[134:135], v[134:135], v[166:167], v[10:11] op_sel_hi:[1,0,1]
	v_pk_fma_f32 v[138:139], v[140:141], v[166:167], v[12:13] op_sel_hi:[1,0,1]
	v_min_f32_e32 v134, 0x40e00000, v134
	v_pk_add_f32 v[2:3], v[144:145], 1.0 op_sel_hi:[1,0]
	v_min_f32_e32 v135, 0x40e00000, v135
	v_rcp_f32_e32 v2, v2
	v_rcp_f32_e32 v3, v3
	v_pk_mul_f32 v[140:141], v[134:135], s[20:21] op_sel_hi:[1,0]
	v_med3_f32 v138, v138, s82, v176
	v_exp_f32_e32 v140, v140
	v_exp_f32_e32 v141, v141
	v_med3_f32 v139, v139, s82, v176
	v_pk_mul_f32 v[2:3], v[142:143], v[2:3]
	v_pk_fma_f32 v[2:3], v[138:139], v[2:3], v[2:3]
	v_pk_fma_f32 v[130:131], v[130:131], v[166:167], v[8:9] op_sel_hi:[1,0,1]
	v_cvt_pk_fp8_f32 v21, v2, v3 op_sel:[0,0,1]
	v_pk_add_f32 v[2:3], v[140:141], 1.0 op_sel_hi:[1,0]
	v_med3_f32 v130, v130, s82, v176
	v_rcp_f32_e32 v2, v2
	v_rcp_f32_e32 v3, v3
	v_med3_f32 v131, v131, s82, v176
	v_pk_fma_f32 v[126:127], v[126:127], v[164:165], v[24:25] op_sel_hi:[1,0,1]
	v_pk_mul_f32 v[2:3], v[134:135], v[2:3]
	v_pk_fma_f32 v[134:135], v[136:137], v[166:167], v[6:7] op_sel_hi:[1,0,1]
	v_pk_fma_f32 v[2:3], v[130:131], v[2:3], v[2:3]
	v_min_f32_e32 v134, 0x40e00000, v134
	v_min_f32_e32 v135, 0x40e00000, v135
	v_pk_mul_f32 v[136:137], v[134:135], s[20:21] op_sel_hi:[1,0]
	v_cvt_pk_fp8_f32 v27, v2, v3
	v_exp_f32_e32 v136, v136
	v_exp_f32_e32 v137, v137
	v_pk_fma_f32 v[130:131], v[132:133], v[166:167], v[4:5] op_sel_hi:[1,0,1]
	v_med3_f32 v130, v130, s82, v176
	v_pk_add_f32 v[2:3], v[136:137], 1.0 op_sel_hi:[1,0]
	v_med3_f32 v131, v131, s82, v176
	v_rcp_f32_e32 v2, v2
	v_rcp_f32_e32 v3, v3
	v_min_f32_e32 v126, 0x40e00000, v126
	v_min_f32_e32 v127, 0x40e00000, v127
	v_pk_mul_f32 v[132:133], v[126:127], s[20:21] op_sel_hi:[1,0]
	v_pk_mul_f32 v[2:3], v[134:135], v[2:3]
	v_exp_f32_e32 v132, v132
	v_pk_fma_f32 v[2:3], v[130:131], v[2:3], v[2:3]
	v_add_u32_e32 v130, 16, v20
	v_cvt_pk_fp8_f32 v27, v2, v3 op_sel:[0,0,1]
	v_ashrrev_i32_e32 v131, 31, v130
	v_lshlrev_b64 v[130:131], 10, v[130:131]
	v_exp_f32_e32 v133, v133
	v_lshl_add_u64 v[130:131], s[12:13], 0, v[130:131]
	v_mov_b32_e32 v2, v21
	v_mov_b32_e32 v3, v27
	v_lshl_add_u64 v[130:131], v[130:131], 0, s[26:27]
	v_lshl_add_u64 v[130:131], v[130:131], 0, v[18:19]
	global_store_dwordx2 v[130:131], v[2:3], off
	v_pk_add_f32 v[2:3], v[132:133], 1.0 op_sel_hi:[1,0]
	v_pk_fma_f32 v[122:123], v[122:123], v[164:165], v[16:17] op_sel_hi:[1,0,1]
	v_rcp_f32_e32 v2, v2
	v_rcp_f32_e32 v3, v3
	v_med3_f32 v122, v122, s82, v176
	v_med3_f32 v123, v123, s82, v176
	v_pk_mul_f32 v[2:3], v[126:127], v[2:3]
	v_pk_fma_f32 v[126:127], v[128:129], v[164:165], v[14:15] op_sel_hi:[1,0,1]
	v_pk_fma_f32 v[2:3], v[122:123], v[2:3], v[2:3]
	v_min_f32_e32 v126, 0x40e00000, v126
	v_min_f32_e32 v127, 0x40e00000, v127
	v_pk_mul_f32 v[128:129], v[126:127], s[20:21] op_sel_hi:[1,0]
	v_cvt_pk_fp8_f32 v21, v2, v3
	v_exp_f32_e32 v128, v128
	v_exp_f32_e32 v129, v129
	v_pk_fma_f32 v[118:119], v[118:119], v[164:165], v[10:11] op_sel_hi:[1,0,1]
	v_pk_fma_f32 v[122:123], v[124:125], v[164:165], v[12:13] op_sel_hi:[1,0,1]
	v_min_f32_e32 v118, 0x40e00000, v118
	v_pk_add_f32 v[2:3], v[128:129], 1.0 op_sel_hi:[1,0]
	v_min_f32_e32 v119, 0x40e00000, v119
	v_rcp_f32_e32 v2, v2
	v_rcp_f32_e32 v3, v3
	v_pk_mul_f32 v[124:125], v[118:119], s[20:21] op_sel_hi:[1,0]
	v_med3_f32 v122, v122, s82, v176
	v_exp_f32_e32 v124, v124
	v_exp_f32_e32 v125, v125
	v_med3_f32 v123, v123, s82, v176
	v_pk_mul_f32 v[2:3], v[126:127], v[2:3]
	v_pk_fma_f32 v[2:3], v[122:123], v[2:3], v[2:3]
	v_pk_fma_f32 v[114:115], v[114:115], v[164:165], v[8:9] op_sel_hi:[1,0,1]
	v_cvt_pk_fp8_f32 v21, v2, v3 op_sel:[0,0,1]
	v_pk_add_f32 v[2:3], v[124:125], 1.0 op_sel_hi:[1,0]
	v_med3_f32 v114, v114, s82, v176
	v_rcp_f32_e32 v2, v2
	v_rcp_f32_e32 v3, v3
	v_med3_f32 v115, v115, s82, v176
	v_pk_fma_f32 v[110:111], v[110:111], v[32:33], v[24:25] op_sel_hi:[1,0,1]
	v_pk_mul_f32 v[2:3], v[118:119], v[2:3]
	v_pk_fma_f32 v[118:119], v[120:121], v[164:165], v[6:7] op_sel_hi:[1,0,1]
	v_pk_fma_f32 v[2:3], v[114:115], v[2:3], v[2:3]
	v_min_f32_e32 v118, 0x40e00000, v118
	v_min_f32_e32 v119, 0x40e00000, v119
	v_pk_mul_f32 v[120:121], v[118:119], s[20:21] op_sel_hi:[1,0]
	v_cvt_pk_fp8_f32 v27, v2, v3
	v_exp_f32_e32 v120, v120
	v_exp_f32_e32 v121, v121
	v_pk_fma_f32 v[114:115], v[116:117], v[164:165], v[4:5] op_sel_hi:[1,0,1]
	v_med3_f32 v114, v114, s82, v176
	v_pk_add_f32 v[2:3], v[120:121], 1.0 op_sel_hi:[1,0]
	v_med3_f32 v115, v115, s82, v176
	v_rcp_f32_e32 v2, v2
	v_rcp_f32_e32 v3, v3
	v_min_f32_e32 v110, 0x40e00000, v110
	v_min_f32_e32 v111, 0x40e00000, v111
	v_pk_mul_f32 v[116:117], v[110:111], s[20:21] op_sel_hi:[1,0]
	v_pk_mul_f32 v[2:3], v[118:119], v[2:3]
	v_exp_f32_e32 v116, v116
	v_pk_fma_f32 v[2:3], v[114:115], v[2:3], v[2:3]
	v_add_u32_e32 v114, 32, v20
	v_cvt_pk_fp8_f32 v27, v2, v3 op_sel:[0,0,1]
	v_ashrrev_i32_e32 v115, 31, v114
	v_lshlrev_b64 v[114:115], 10, v[114:115]
	v_exp_f32_e32 v117, v117
	v_lshl_add_u64 v[114:115], s[12:13], 0, v[114:115]
	v_mov_b32_e32 v2, v21
	v_mov_b32_e32 v3, v27
	v_lshl_add_u64 v[114:115], v[114:115], 0, s[26:27]
	v_lshl_add_u64 v[114:115], v[114:115], 0, v[18:19]
	global_store_dwordx2 v[114:115], v[2:3], off
	v_pk_add_f32 v[2:3], v[116:117], 1.0 op_sel_hi:[1,0]
	v_pk_fma_f32 v[106:107], v[106:107], v[32:33], v[16:17] op_sel_hi:[1,0,1]
	v_rcp_f32_e32 v2, v2
	v_rcp_f32_e32 v3, v3
	v_med3_f32 v106, v106, s82, v176
	v_med3_f32 v107, v107, s82, v176
	v_pk_mul_f32 v[2:3], v[110:111], v[2:3]
	v_pk_fma_f32 v[110:111], v[112:113], v[32:33], v[14:15] op_sel_hi:[1,0,1]
	v_pk_fma_f32 v[2:3], v[106:107], v[2:3], v[2:3]
	v_min_f32_e32 v110, 0x40e00000, v110
	v_min_f32_e32 v111, 0x40e00000, v111
	v_pk_mul_f32 v[112:113], v[110:111], s[20:21] op_sel_hi:[1,0]
	v_cvt_pk_fp8_f32 v21, v2, v3
	v_exp_f32_e32 v112, v112
	v_exp_f32_e32 v113, v113
	v_pk_fma_f32 v[102:103], v[102:103], v[32:33], v[10:11] op_sel_hi:[1,0,1]
	v_pk_fma_f32 v[106:107], v[108:109], v[32:33], v[12:13] op_sel_hi:[1,0,1]
	v_min_f32_e32 v102, 0x40e00000, v102
	v_pk_add_f32 v[2:3], v[112:113], 1.0 op_sel_hi:[1,0]
	v_min_f32_e32 v103, 0x40e00000, v103
	v_rcp_f32_e32 v2, v2
	v_rcp_f32_e32 v3, v3
	v_pk_mul_f32 v[108:109], v[102:103], s[20:21] op_sel_hi:[1,0]
	v_med3_f32 v106, v106, s82, v176
	v_exp_f32_e32 v108, v108
	v_exp_f32_e32 v109, v109
	v_med3_f32 v107, v107, s82, v176
	v_pk_mul_f32 v[2:3], v[110:111], v[2:3]
	v_pk_fma_f32 v[2:3], v[106:107], v[2:3], v[2:3]
	v_pk_fma_f32 v[98:99], v[98:99], v[32:33], v[8:9] op_sel_hi:[1,0,1]
	v_cvt_pk_fp8_f32 v21, v2, v3 op_sel:[0,0,1]
	v_pk_add_f32 v[2:3], v[108:109], 1.0 op_sel_hi:[1,0]
	v_med3_f32 v98, v98, s82, v176
	v_rcp_f32_e32 v2, v2
	v_rcp_f32_e32 v3, v3
	v_med3_f32 v99, v99, s82, v176
	v_pk_fma_f32 v[94:95], v[94:95], v[30:31], v[24:25] op_sel_hi:[1,0,1]
	v_pk_mul_f32 v[2:3], v[102:103], v[2:3]
	v_pk_fma_f32 v[102:103], v[104:105], v[32:33], v[6:7] op_sel_hi:[1,0,1]
	v_pk_fma_f32 v[2:3], v[98:99], v[2:3], v[2:3]
	v_min_f32_e32 v102, 0x40e00000, v102
	v_min_f32_e32 v103, 0x40e00000, v103
	v_pk_mul_f32 v[104:105], v[102:103], s[20:21] op_sel_hi:[1,0]
	v_cvt_pk_fp8_f32 v27, v2, v3
	v_exp_f32_e32 v104, v104
	v_exp_f32_e32 v105, v105
	v_pk_fma_f32 v[32:33], v[100:101], v[32:33], v[4:5] op_sel_hi:[1,0,1]
	v_med3_f32 v32, v32, s82, v176
	v_pk_add_f32 v[2:3], v[104:105], 1.0 op_sel_hi:[1,0]
	v_med3_f32 v33, v33, s82, v176
	v_rcp_f32_e32 v2, v2
	v_rcp_f32_e32 v3, v3
	v_min_f32_e32 v94, 0x40e00000, v94
	v_min_f32_e32 v95, 0x40e00000, v95
	v_pk_mul_f32 v[98:99], v[94:95], s[20:21] op_sel_hi:[1,0]
	v_pk_mul_f32 v[2:3], v[102:103], v[2:3]
	v_exp_f32_e32 v98, v98
	v_pk_fma_f32 v[2:3], v[32:33], v[2:3], v[2:3]
	v_add_u32_e32 v32, 48, v20
	v_cvt_pk_fp8_f32 v27, v2, v3 op_sel:[0,0,1]
	v_ashrrev_i32_e32 v33, 31, v32
	v_lshlrev_b64 v[32:33], 10, v[32:33]
	v_exp_f32_e32 v99, v99
	v_lshl_add_u64 v[32:33], s[12:13], 0, v[32:33]
	v_mov_b32_e32 v2, v21
	v_mov_b32_e32 v3, v27
	v_lshl_add_u64 v[32:33], v[32:33], 0, s[26:27]
	v_lshl_add_u64 v[32:33], v[32:33], 0, v[18:19]
	global_store_dwordx2 v[32:33], v[2:3], off
	v_pk_add_f32 v[32:33], v[98:99], 1.0 op_sel_hi:[1,0]
	v_pk_fma_f32 v[90:91], v[90:91], v[30:31], v[16:17] op_sel_hi:[1,0,1]
	v_rcp_f32_e32 v32, v32
	v_rcp_f32_e32 v33, v33
	v_med3_f32 v90, v90, s82, v176
	v_med3_f32 v91, v91, s82, v176
	v_pk_mul_f32 v[32:33], v[94:95], v[32:33]
	v_pk_fma_f32 v[94:95], v[96:97], v[30:31], v[14:15] op_sel_hi:[1,0,1]
	v_pk_fma_f32 v[32:33], v[90:91], v[32:33], v[32:33]
	v_min_f32_e32 v94, 0x40e00000, v94
	v_min_f32_e32 v95, 0x40e00000, v95
	v_pk_mul_f32 v[96:97], v[94:95], s[20:21] op_sel_hi:[1,0]
	v_cvt_pk_fp8_f32 v3, v32, v33
	v_exp_f32_e32 v96, v96
	v_exp_f32_e32 v97, v97
	v_pk_fma_f32 v[86:87], v[86:87], v[30:31], v[10:11] op_sel_hi:[1,0,1]
	v_pk_fma_f32 v[90:91], v[92:93], v[30:31], v[12:13] op_sel_hi:[1,0,1]
	v_min_f32_e32 v86, 0x40e00000, v86
	v_pk_add_f32 v[32:33], v[96:97], 1.0 op_sel_hi:[1,0]
	v_min_f32_e32 v87, 0x40e00000, v87
	v_rcp_f32_e32 v32, v32
	v_rcp_f32_e32 v33, v33
	v_pk_mul_f32 v[92:93], v[86:87], s[20:21] op_sel_hi:[1,0]
	v_med3_f32 v90, v90, s82, v176
	v_exp_f32_e32 v92, v92
	v_exp_f32_e32 v93, v93
	v_med3_f32 v91, v91, s82, v176
	v_pk_mul_f32 v[32:33], v[94:95], v[32:33]
	v_pk_fma_f32 v[32:33], v[90:91], v[32:33], v[32:33]
	v_pk_fma_f32 v[82:83], v[82:83], v[30:31], v[8:9] op_sel_hi:[1,0,1]
	v_cvt_pk_fp8_f32 v3, v32, v33 op_sel:[0,0,1]
	v_pk_add_f32 v[32:33], v[92:93], 1.0 op_sel_hi:[1,0]
	v_med3_f32 v82, v82, s82, v176
	v_rcp_f32_e32 v32, v32
	v_rcp_f32_e32 v33, v33
	v_med3_f32 v83, v83, s82, v176
	v_add_u32_e32 v2, 0x80, v20
	v_pk_mul_f32 v[32:33], v[86:87], v[32:33]
	v_pk_fma_f32 v[86:87], v[88:89], v[30:31], v[6:7] op_sel_hi:[1,0,1]
	v_pk_fma_f32 v[32:33], v[82:83], v[32:33], v[32:33]
	v_min_f32_e32 v86, 0x40e00000, v86
	v_min_f32_e32 v87, 0x40e00000, v87
	v_pk_mul_f32 v[88:89], v[86:87], s[20:21] op_sel_hi:[1,0]
	v_cvt_pk_fp8_f32 v23, v32, v33
	v_exp_f32_e32 v88, v88
	v_exp_f32_e32 v89, v89
	v_pk_fma_f32 v[30:31], v[84:85], v[30:31], v[4:5] op_sel_hi:[1,0,1]
	v_med3_f32 v30, v30, s82, v176
	v_pk_add_f32 v[32:33], v[88:89], 1.0 op_sel_hi:[1,0]
	v_med3_f32 v31, v31, s82, v176
	v_rcp_f32_e32 v32, v32
	v_rcp_f32_e32 v33, v33
	s_and_b64 vcc, exec, s[4:5]
	v_pk_mul_f32 v[32:33], v[86:87], v[32:33]
	s_mov_b64 s[4:5], -1
	v_pk_fma_f32 v[30:31], v[30:31], v[32:33], v[32:33]
	v_pk_fma_f32 v[32:33], v[78:79], v[28:29], v[24:25] op_sel_hi:[1,0,1]
	v_cvt_pk_fp8_f32 v23, v30, v31 op_sel:[0,0,1]
	v_min_f32_e32 v32, 0x40e00000, v32
	v_min_f32_e32 v33, 0x40e00000, v33
	v_mov_b32_e32 v30, v3
	v_ashrrev_i32_e32 v3, 31, v2
	v_pk_mul_f32 v[78:79], v[32:33], s[20:21] op_sel_hi:[1,0]
	v_lshlrev_b64 v[2:3], 10, v[2:3]
	v_exp_f32_e32 v78, v78
	v_exp_f32_e32 v79, v79
	v_lshl_add_u64 v[2:3], s[12:13], 0, v[2:3]
	v_lshl_add_u64 v[2:3], v[2:3], 0, s[26:27]
	v_mov_b32_e32 v31, v23
	v_lshl_add_u64 v[2:3], v[2:3], 0, v[18:19]
	global_store_dwordx2 v[2:3], v[30:31], off
	v_pk_add_f32 v[2:3], v[78:79], 1.0 op_sel_hi:[1,0]
	v_pk_fma_f32 v[30:31], v[74:75], v[28:29], v[16:17] op_sel_hi:[1,0,1]
	v_rcp_f32_e32 v2, v2
	v_rcp_f32_e32 v3, v3
	v_med3_f32 v30, v30, s82, v176
	v_med3_f32 v31, v31, s82, v176
	v_pk_mul_f32 v[2:3], v[32:33], v[2:3]
	v_pk_fma_f32 v[32:33], v[80:81], v[28:29], v[14:15] op_sel_hi:[1,0,1]
	v_pk_fma_f32 v[2:3], v[30:31], v[2:3], v[2:3]
	v_min_f32_e32 v32, 0x40e00000, v32
	v_min_f32_e32 v33, 0x40e00000, v33
	v_pk_mul_f32 v[74:75], v[32:33], s[20:21] op_sel_hi:[1,0]
	v_cvt_pk_fp8_f32 v21, v2, v3
	v_exp_f32_e32 v74, v74
	v_exp_f32_e32 v75, v75
	v_pk_fma_f32 v[30:31], v[76:77], v[28:29], v[12:13] op_sel_hi:[1,0,1]
	v_med3_f32 v30, v30, s82, v176
	v_pk_add_f32 v[2:3], v[74:75], 1.0 op_sel_hi:[1,0]
	v_med3_f32 v31, v31, s82, v176
	v_rcp_f32_e32 v2, v2
	v_rcp_f32_e32 v3, v3
	s_nop 0
	v_pk_mul_f32 v[2:3], v[32:33], v[2:3]
	v_pk_fma_f32 v[32:33], v[70:71], v[28:29], v[10:11] op_sel_hi:[1,0,1]
	v_pk_fma_f32 v[2:3], v[30:31], v[2:3], v[2:3]
	v_min_f32_e32 v32, 0x40e00000, v32
	v_min_f32_e32 v33, 0x40e00000, v33
	v_pk_mul_f32 v[70:71], v[32:33], s[20:21] op_sel_hi:[1,0]
	v_cvt_pk_fp8_f32 v21, v2, v3 op_sel:[0,0,1]
	v_exp_f32_e32 v70, v70
	v_exp_f32_e32 v71, v71
	v_pk_fma_f32 v[30:31], v[66:67], v[28:29], v[8:9] op_sel_hi:[1,0,1]
	v_pk_add_f32 v[2:3], v[70:71], 1.0 op_sel_hi:[1,0]
	s_nop 0
	v_rcp_f32_e32 v2, v2
	v_rcp_f32_e32 v3, v3
	v_med3_f32 v30, v30, s82, v176
	v_med3_f32 v31, v31, s82, v176
	v_pk_mul_f32 v[2:3], v[32:33], v[2:3]
	v_pk_fma_f32 v[32:33], v[72:73], v[28:29], v[6:7] op_sel_hi:[1,0,1]
	v_pk_fma_f32 v[2:3], v[30:31], v[2:3], v[2:3]
	v_min_f32_e32 v32, 0x40e00000, v32
	v_min_f32_e32 v33, 0x40e00000, v33
	v_pk_mul_f32 v[66:67], v[32:33], s[20:21] op_sel_hi:[1,0]
	v_cvt_pk_fp8_f32 v27, v2, v3
	v_exp_f32_e32 v66, v66
	v_exp_f32_e32 v67, v67
	v_pk_fma_f32 v[28:29], v[68:69], v[28:29], v[4:5] op_sel_hi:[1,0,1]
	v_pk_fma_f32 v[30:31], v[62:63], v[26:27], v[24:25] op_sel_hi:[1,0,1]
	v_med3_f32 v28, v28, s82, v176
	v_pk_add_f32 v[2:3], v[66:67], 1.0 op_sel_hi:[1,0]
	v_med3_f32 v29, v29, s82, v176
	v_rcp_f32_e32 v2, v2
	v_rcp_f32_e32 v3, v3
	v_min_f32_e32 v30, 0x40e00000, v30
	v_min_f32_e32 v31, 0x40e00000, v31
	v_pk_mul_f32 v[2:3], v[32:33], v[2:3]
	s_nop 0
	v_pk_fma_f32 v[2:3], v[28:29], v[2:3], v[2:3]
	v_cvt_pk_fp8_f32 v27, v2, v3 op_sel:[0,0,1]
	s_nop 0
	v_mov_b32_e32 v3, v27
	v_pk_mul_f32 v[32:33], v[30:31], s[20:21] op_sel_hi:[1,0]
	v_mov_b32_e32 v2, v21
	v_add_u32_e32 v28, 0x90, v20
	v_ashrrev_i32_e32 v29, 31, v28
	v_lshlrev_b64 v[28:29], 10, v[28:29]
	v_exp_f32_e32 v32, v32
	v_exp_f32_e32 v33, v33
	v_lshl_add_u64 v[28:29], s[12:13], 0, v[28:29]
	v_lshl_add_u64 v[28:29], v[28:29], 0, s[26:27]
	v_lshl_add_u64 v[28:29], v[28:29], 0, v[18:19]
	global_store_dwordx2 v[28:29], v[2:3], off
	v_pk_add_f32 v[2:3], v[32:33], 1.0 op_sel_hi:[1,0]
	v_pk_fma_f32 v[28:29], v[58:59], v[26:27], v[16:17] op_sel_hi:[1,0,1]
	v_rcp_f32_e32 v2, v2
	v_rcp_f32_e32 v3, v3
	v_med3_f32 v28, v28, s82, v176
	v_med3_f32 v29, v29, s82, v176
	v_pk_mul_f32 v[2:3], v[30:31], v[2:3]
	v_pk_fma_f32 v[30:31], v[64:65], v[26:27], v[14:15] op_sel_hi:[1,0,1]
	v_pk_fma_f32 v[2:3], v[28:29], v[2:3], v[2:3]
	v_min_f32_e32 v30, 0x40e00000, v30
	v_min_f32_e32 v31, 0x40e00000, v31
	v_pk_mul_f32 v[32:33], v[30:31], s[20:21] op_sel_hi:[1,0]
	v_cvt_pk_fp8_f32 v21, v2, v3
	v_exp_f32_e32 v32, v32
	v_exp_f32_e32 v33, v33
	v_pk_fma_f32 v[28:29], v[60:61], v[26:27], v[12:13] op_sel_hi:[1,0,1]
	v_med3_f32 v28, v28, s82, v176
	v_pk_add_f32 v[2:3], v[32:33], 1.0 op_sel_hi:[1,0]
	v_med3_f32 v29, v29, s82, v176
	v_rcp_f32_e32 v2, v2
	v_rcp_f32_e32 v3, v3
	s_nop 0
	v_pk_mul_f32 v[2:3], v[30:31], v[2:3]
	v_pk_fma_f32 v[30:31], v[54:55], v[26:27], v[10:11] op_sel_hi:[1,0,1]
	v_pk_fma_f32 v[2:3], v[28:29], v[2:3], v[2:3]
	v_min_f32_e32 v30, 0x40e00000, v30
	v_min_f32_e32 v31, 0x40e00000, v31
	v_pk_mul_f32 v[32:33], v[30:31], s[20:21] op_sel_hi:[1,0]
	v_cvt_pk_fp8_f32 v21, v2, v3 op_sel:[0,0,1]
	v_exp_f32_e32 v32, v32
	v_exp_f32_e32 v33, v33
	v_pk_fma_f32 v[28:29], v[50:51], v[26:27], v[8:9] op_sel_hi:[1,0,1]
	v_pk_fma_f32 v[24:25], v[46:47], v[22:23], v[24:25] op_sel_hi:[1,0,1]
	v_med3_f32 v28, v28, s82, v176
	v_pk_add_f32 v[2:3], v[32:33], 1.0 op_sel_hi:[1,0]
	v_med3_f32 v29, v29, s82, v176
	v_rcp_f32_e32 v2, v2
	v_rcp_f32_e32 v3, v3
	v_min_f32_e32 v24, 0x40e00000, v24
	v_min_f32_e32 v25, 0x40e00000, v25
	v_pk_fma_f32 v[14:15], v[48:49], v[22:23], v[14:15] op_sel_hi:[1,0,1]
	v_pk_mul_f32 v[2:3], v[30:31], v[2:3]
	v_pk_fma_f32 v[30:31], v[56:57], v[26:27], v[6:7] op_sel_hi:[1,0,1]
	v_pk_fma_f32 v[2:3], v[28:29], v[2:3], v[2:3]
	v_min_f32_e32 v30, 0x40e00000, v30
	v_min_f32_e32 v31, 0x40e00000, v31
	v_pk_mul_f32 v[32:33], v[30:31], s[20:21] op_sel_hi:[1,0]
	v_exp_f32_e32 v32, v32
	v_exp_f32_e32 v33, v33
	v_cvt_pk_fp8_f32 v28, v2, v3
	v_pk_fma_f32 v[26:27], v[52:53], v[26:27], v[4:5] op_sel_hi:[1,0,1]
	v_min_f32_e32 v14, 0x40e00000, v14
	v_pk_add_f32 v[2:3], v[32:33], 1.0 op_sel_hi:[1,0]
	v_med3_f32 v26, v26, s82, v176
	v_rcp_f32_e32 v2, v2
	v_rcp_f32_e32 v3, v3
	v_med3_f32 v27, v27, s82, v176
	v_min_f32_e32 v15, 0x40e00000, v15
	v_pk_fma_f32 v[16:17], v[42:43], v[22:23], v[16:17] op_sel_hi:[1,0,1]
	v_pk_mul_f32 v[2:3], v[30:31], v[2:3]
	v_med3_f32 v16, v16, s82, v176
	v_pk_fma_f32 v[2:3], v[26:27], v[2:3], v[2:3]
	v_cvt_pk_fp8_f32 v28, v2, v3 op_sel:[0,0,1]
	s_nop 0
	v_mov_b32_e32 v3, v28
	v_pk_mul_f32 v[28:29], v[24:25], s[20:21] op_sel_hi:[1,0]
	v_mov_b32_e32 v2, v21
	v_add_u32_e32 v26, 0xa0, v20
	v_ashrrev_i32_e32 v27, 31, v26
	v_lshlrev_b64 v[26:27], 10, v[26:27]
	v_exp_f32_e32 v28, v28
	v_exp_f32_e32 v29, v29
	v_lshl_add_u64 v[26:27], s[12:13], 0, v[26:27]
	v_lshl_add_u64 v[26:27], v[26:27], 0, s[26:27]
	v_lshl_add_u64 v[26:27], v[26:27], 0, v[18:19]
	global_store_dwordx2 v[26:27], v[2:3], off
	v_pk_add_f32 v[2:3], v[28:29], 1.0 op_sel_hi:[1,0]
	v_med3_f32 v17, v17, s82, v176
	v_rcp_f32_e32 v2, v2
	v_rcp_f32_e32 v3, v3
	v_pk_fma_f32 v[10:11], v[38:39], v[22:23], v[10:11] op_sel_hi:[1,0,1]
	v_pk_fma_f32 v[12:13], v[44:45], v[22:23], v[12:13] op_sel_hi:[1,0,1]
	v_min_f32_e32 v10, 0x40e00000, v10
	v_pk_mul_f32 v[2:3], v[24:25], v[2:3]
	v_pk_mul_f32 v[24:25], v[14:15], s[20:21] op_sel_hi:[1,0]
	v_pk_fma_f32 v[2:3], v[16:17], v[2:3], v[2:3]
	v_exp_f32_e32 v24, v24
	v_exp_f32_e32 v25, v25
	v_cvt_pk_fp8_f32 v16, v2, v3
	v_min_f32_e32 v11, 0x40e00000, v11
	v_pk_add_f32 v[2:3], v[24:25], 1.0 op_sel_hi:[1,0]
	v_med3_f32 v12, v12, s82, v176
	v_rcp_f32_e32 v2, v2
	v_rcp_f32_e32 v3, v3
	v_med3_f32 v13, v13, s82, v176
	v_pk_fma_f32 v[6:7], v[40:41], v[22:23], v[6:7] op_sel_hi:[1,0,1]
	v_pk_fma_f32 v[8:9], v[34:35], v[22:23], v[8:9] op_sel_hi:[1,0,1]
	v_pk_mul_f32 v[2:3], v[14:15], v[2:3]
	v_pk_mul_f32 v[14:15], v[10:11], s[20:21] op_sel_hi:[1,0]
	v_pk_fma_f32 v[2:3], v[12:13], v[2:3], v[2:3]
	v_exp_f32_e32 v14, v14
	v_exp_f32_e32 v15, v15
	v_cvt_pk_fp8_f32 v16, v2, v3 op_sel:[0,0,1]
	v_min_f32_e32 v6, 0x40e00000, v6
	v_pk_add_f32 v[2:3], v[14:15], 1.0 op_sel_hi:[1,0]
	v_min_f32_e32 v7, 0x40e00000, v7
	v_rcp_f32_e32 v2, v2
	v_rcp_f32_e32 v3, v3
	v_med3_f32 v8, v8, s82, v176
	v_med3_f32 v9, v9, s82, v176
	v_pk_fma_f32 v[4:5], v[36:37], v[22:23], v[4:5] op_sel_hi:[1,0,1]
	v_pk_mul_f32 v[2:3], v[10:11], v[2:3]
	v_pk_mul_f32 v[10:11], v[6:7], s[20:21] op_sel_hi:[1,0]
	v_pk_fma_f32 v[2:3], v[8:9], v[2:3], v[2:3]
	v_exp_f32_e32 v10, v10
	v_exp_f32_e32 v11, v11
	v_cvt_pk_fp8_f32 v8, v2, v3
	v_med3_f32 v4, v4, s82, v176
	v_pk_add_f32 v[2:3], v[10:11], 1.0 op_sel_hi:[1,0]
	v_med3_f32 v5, v5, s82, v176
	v_rcp_f32_e32 v2, v2
	v_rcp_f32_e32 v3, v3
	s_nop 0
	v_pk_mul_f32 v[2:3], v[6:7], v[2:3]
	s_nop 0
	v_pk_fma_f32 v[2:3], v[4:5], v[2:3], v[2:3]
	v_cvt_pk_fp8_f32 v8, v2, v3 op_sel:[0,0,1]
	s_nop 0
	v_mov_b32_e32 v3, v8
	v_mov_b32_e32 v2, v16
	v_add_u32_e32 v4, 0xb0, v20
	v_ashrrev_i32_e32 v5, 31, v4
	v_lshlrev_b64 v[4:5], 10, v[4:5]
	v_lshl_add_u64 v[4:5], s[12:13], 0, v[4:5]
	v_lshl_add_u64 v[4:5], v[4:5], 0, s[26:27]
	v_lshl_add_u64 v[4:5], v[4:5], 0, v[18:19]
	global_store_dwordx2 v[4:5], v[2:3], off
	s_cbranch_vccnz .LBB0_1937
	s_andn2_b64 vcc, exec, s[14:15]
	s_cbranch_vccnz .LBB0_1936
	s_barrier
	s_branch .LBB0_1936
